# stream hand-structured: 10 x 1KiB loads in flight per wave (ring of slots), rotated wave-row assignment, baseline row mapping
# speedup vs baseline: 1.0245x; 1.0245x over previous
.Lst_nou:
	s_or_b64 exec, exec, s[0:1]
	s_lshr_b32 s8, s3, 6
	v_and_b32_e32 v63, 63, v0
	v_lshlrev_b32_e32 v64, 4, v63
	s_add_i32 s8, s8, s2
	s_and_b32 s8, s8, 15
	s_lshl_b32 s11, s2, 7
	s_lshl_b32 s24, s2, 5
	s_add_i32 s11, s11, s8
	s_lshl_b32 s16, s11, 12
	s_add_i32 s17, s16, 0x10000
	s_add_i32 s18, s16, 0x20000
	s_add_i32 s19, s16, 0x30000
	s_add_i32 s20, s16, 0x40000
	s_add_i32 s21, s16, 0x50000
	s_add_i32 s22, s16, 0x60000
	s_add_i32 s23, s16, 0x70000
	s_waitcnt lgkmcnt(0)
	s_mov_b32 s0, s4
	s_and_b32 s1, s5, 0xffff
	s_brev_b32 s2, 16
	s_mov_b32 s3, 0x20000
	buffer_load_dwordx4 v[16:19], v64, s[0:3], s16 offen nt
	buffer_load_dwordx4 v[20:23], v64, s[0:3], s16 offen offset:1024 nt
	buffer_load_dwordx4 v[24:27], v64, s[0:3], s16 offen offset:2048 nt
	buffer_load_dwordx4 v[28:31], v64, s[0:3], s16 offen offset:3072 nt
	buffer_load_dwordx4 v[32:35], v64, s[0:3], s17 offen nt
	buffer_load_dwordx4 v[36:39], v64, s[0:3], s17 offen offset:1024 nt
	buffer_load_dwordx4 v[40:43], v64, s[0:3], s17 offen offset:2048 nt
	buffer_load_dwordx4 v[44:47], v64, s[0:3], s17 offen offset:3072 nt
	s_barrier
	buffer_load_dwordx4 v[48:51], v64, s[0:3], s18 offen nt
	buffer_load_dwordx4 v[52:55], v64, s[0:3], s18 offen offset:1024 nt
	ds_read_b128 v[0:3], v64
	ds_read_b128 v[4:7], v64 offset:1024
	ds_read_b128 v[8:11], v64 offset:2048
	ds_read_b128 v[12:15], v64 offset:3072
	v_mov_b32_e32 v62, 0
	s_waitcnt lgkmcnt(0)
	s_waitcnt vmcnt(9)
	v_pk_mul_f32 v[56:57], v[16:17], v[0:1]
	v_pk_mul_f32 v[58:59], v[18:19], v[2:3]
	buffer_load_dwordx4 v[16:19], v64, s[0:3], s18 offen offset:2048 nt
	s_waitcnt vmcnt(9)
	v_pk_fma_f32 v[56:57], v[20:21], v[4:5], v[56:57]
	v_pk_fma_f32 v[58:59], v[22:23], v[6:7], v[58:59]
	buffer_load_dwordx4 v[20:23], v64, s[0:3], s18 offen offset:3072 nt
	s_waitcnt vmcnt(9)
	v_pk_fma_f32 v[56:57], v[24:25], v[8:9], v[56:57]
	v_pk_fma_f32 v[58:59], v[26:27], v[10:11], v[58:59]
	buffer_load_dwordx4 v[24:27], v64, s[0:3], s19 offen nt
	s_waitcnt vmcnt(9)
	v_pk_fma_f32 v[56:57], v[28:29], v[12:13], v[56:57]
	v_pk_fma_f32 v[58:59], v[30:31], v[14:15], v[58:59]
	buffer_load_dwordx4 v[28:31], v64, s[0:3], s19 offen offset:1024 nt
	v_pk_add_f32 v[56:57], v[56:57], v[58:59]
	v_cmp_eq_u32_e32 vcc, 0, v63
	v_add_f32_e32 v60, v56, v57
	s_nop 1
	v_add_f32_dpp v60, v60, v60 quad_perm:[1,0,3,2] row_mask:0xf bank_mask:0xf bound_ctrl:1
	s_nop 1
	v_add_f32_dpp v60, v60, v60 quad_perm:[2,3,0,1] row_mask:0xf bank_mask:0xf bound_ctrl:1
	s_nop 1
	v_add_f32_dpp v60, v60, v60 row_ror:4 row_mask:0xf bank_mask:0xf bound_ctrl:1
	s_nop 1
	v_add_f32_dpp v60, v60, v60 row_ror:8 row_mask:0xf bank_mask:0xf bound_ctrl:1
	v_mov_b32_e32 v61, v60
	s_nop 1
	v_permlane16_swap_b32_e32 v60, v61
	v_add_f32_e32 v60, v60, v61
	v_mov_b32_e32 v61, v60
	s_nop 1
	v_permlane32_swap_b32_e32 v60, v61
	v_add_f32_e32 v60, v60, v61
	v_cndmask_b32_e32 v62, v62, v60, vcc
	s_waitcnt vmcnt(9)
	v_pk_mul_f32 v[56:57], v[32:33], v[0:1]
	v_pk_mul_f32 v[58:59], v[34:35], v[2:3]
	buffer_load_dwordx4 v[32:35], v64, s[0:3], s19 offen offset:2048 nt
	s_waitcnt vmcnt(9)
	v_pk_fma_f32 v[56:57], v[36:37], v[4:5], v[56:57]
	v_pk_fma_f32 v[58:59], v[38:39], v[6:7], v[58:59]
	buffer_load_dwordx4 v[36:39], v64, s[0:3], s19 offen offset:3072 nt
	s_waitcnt vmcnt(9)
	v_pk_fma_f32 v[56:57], v[40:41], v[8:9], v[56:57]
	v_pk_fma_f32 v[58:59], v[42:43], v[10:11], v[58:59]
	buffer_load_dwordx4 v[40:43], v64, s[0:3], s20 offen nt
	s_waitcnt vmcnt(9)
	v_pk_fma_f32 v[56:57], v[44:45], v[12:13], v[56:57]
	v_pk_fma_f32 v[58:59], v[46:47], v[14:15], v[58:59]
	buffer_load_dwordx4 v[44:47], v64, s[0:3], s20 offen offset:1024 nt
	v_pk_add_f32 v[56:57], v[56:57], v[58:59]
	v_cmp_eq_u32_e32 vcc, 1, v63
	v_add_f32_e32 v60, v56, v57
	s_nop 1
	v_add_f32_dpp v60, v60, v60 quad_perm:[1,0,3,2] row_mask:0xf bank_mask:0xf bound_ctrl:1
	s_nop 1
	v_add_f32_dpp v60, v60, v60 quad_perm:[2,3,0,1] row_mask:0xf bank_mask:0xf bound_ctrl:1
	s_nop 1
	v_add_f32_dpp v60, v60, v60 row_ror:4 row_mask:0xf bank_mask:0xf bound_ctrl:1
	s_nop 1
	v_add_f32_dpp v60, v60, v60 row_ror:8 row_mask:0xf bank_mask:0xf bound_ctrl:1
	v_mov_b32_e32 v61, v60
	s_nop 1
	v_permlane16_swap_b32_e32 v60, v61
	v_add_f32_e32 v60, v60, v61
	v_mov_b32_e32 v61, v60
	s_nop 1
	v_permlane32_swap_b32_e32 v60, v61
	v_add_f32_e32 v60, v60, v61
	v_cndmask_b32_e32 v62, v62, v60, vcc
	s_waitcnt vmcnt(9)
	v_pk_mul_f32 v[56:57], v[48:49], v[0:1]
	v_pk_mul_f32 v[58:59], v[50:51], v[2:3]
	buffer_load_dwordx4 v[48:51], v64, s[0:3], s20 offen offset:2048 nt
	s_waitcnt vmcnt(9)
	v_pk_fma_f32 v[56:57], v[52:53], v[4:5], v[56:57]
	v_pk_fma_f32 v[58:59], v[54:55], v[6:7], v[58:59]
	buffer_load_dwordx4 v[52:55], v64, s[0:3], s20 offen offset:3072 nt
	s_waitcnt vmcnt(9)
	v_pk_fma_f32 v[56:57], v[16:17], v[8:9], v[56:57]
	v_pk_fma_f32 v[58:59], v[18:19], v[10:11], v[58:59]
	buffer_load_dwordx4 v[16:19], v64, s[0:3], s21 offen nt
	s_waitcnt vmcnt(9)
	v_pk_fma_f32 v[56:57], v[20:21], v[12:13], v[56:57]
	v_pk_fma_f32 v[58:59], v[22:23], v[14:15], v[58:59]
	buffer_load_dwordx4 v[20:23], v64, s[0:3], s21 offen offset:1024 nt
	v_pk_add_f32 v[56:57], v[56:57], v[58:59]
	v_cmp_eq_u32_e32 vcc, 2, v63
	v_add_f32_e32 v60, v56, v57
	s_nop 1
	v_add_f32_dpp v60, v60, v60 quad_perm:[1,0,3,2] row_mask:0xf bank_mask:0xf bound_ctrl:1
	s_nop 1
	v_add_f32_dpp v60, v60, v60 quad_perm:[2,3,0,1] row_mask:0xf bank_mask:0xf bound_ctrl:1
	s_nop 1
	v_add_f32_dpp v60, v60, v60 row_ror:4 row_mask:0xf bank_mask:0xf bound_ctrl:1
	s_nop 1
	v_add_f32_dpp v60, v60, v60 row_ror:8 row_mask:0xf bank_mask:0xf bound_ctrl:1
	v_mov_b32_e32 v61, v60
	s_nop 1
	v_permlane16_swap_b32_e32 v60, v61
	v_add_f32_e32 v60, v60, v61
	v_mov_b32_e32 v61, v60
	s_nop 1
	v_permlane32_swap_b32_e32 v60, v61
	v_add_f32_e32 v60, v60, v61
	v_cndmask_b32_e32 v62, v62, v60, vcc
	s_waitcnt vmcnt(9)
	v_pk_mul_f32 v[56:57], v[24:25], v[0:1]
	v_pk_mul_f32 v[58:59], v[26:27], v[2:3]
	buffer_load_dwordx4 v[24:27], v64, s[0:3], s21 offen offset:2048 nt
	s_waitcnt vmcnt(9)
	v_pk_fma_f32 v[56:57], v[28:29], v[4:5], v[56:57]
	v_pk_fma_f32 v[58:59], v[30:31], v[6:7], v[58:59]
	buffer_load_dwordx4 v[28:31], v64, s[0:3], s21 offen offset:3072 nt
	s_waitcnt vmcnt(9)
	v_pk_fma_f32 v[56:57], v[32:33], v[8:9], v[56:57]
	v_pk_fma_f32 v[58:59], v[34:35], v[10:11], v[58:59]
	buffer_load_dwordx4 v[32:35], v64, s[0:3], s22 offen nt
	s_waitcnt vmcnt(9)
	v_pk_fma_f32 v[56:57], v[36:37], v[12:13], v[56:57]
	v_pk_fma_f32 v[58:59], v[38:39], v[14:15], v[58:59]
	buffer_load_dwordx4 v[36:39], v64, s[0:3], s22 offen offset:1024 nt
	v_pk_add_f32 v[56:57], v[56:57], v[58:59]
	v_cmp_eq_u32_e32 vcc, 3, v63
	v_add_f32_e32 v60, v56, v57
	s_nop 1
	v_add_f32_dpp v60, v60, v60 quad_perm:[1,0,3,2] row_mask:0xf bank_mask:0xf bound_ctrl:1
	s_nop 1
	v_add_f32_dpp v60, v60, v60 quad_perm:[2,3,0,1] row_mask:0xf bank_mask:0xf bound_ctrl:1
	s_nop 1
	v_add_f32_dpp v60, v60, v60 row_ror:4 row_mask:0xf bank_mask:0xf bound_ctrl:1
	s_nop 1
	v_add_f32_dpp v60, v60, v60 row_ror:8 row_mask:0xf bank_mask:0xf bound_ctrl:1
	v_mov_b32_e32 v61, v60
	s_nop 1
	v_permlane16_swap_b32_e32 v60, v61
	v_add_f32_e32 v60, v60, v61
	v_mov_b32_e32 v61, v60
	s_nop 1
	v_permlane32_swap_b32_e32 v60, v61
	v_add_f32_e32 v60, v60, v61
	v_cndmask_b32_e32 v62, v62, v60, vcc
	s_waitcnt vmcnt(9)
	v_pk_mul_f32 v[56:57], v[40:41], v[0:1]
	v_pk_mul_f32 v[58:59], v[42:43], v[2:3]
	buffer_load_dwordx4 v[40:43], v64, s[0:3], s22 offen offset:2048 nt
	s_waitcnt vmcnt(9)
	v_pk_fma_f32 v[56:57], v[44:45], v[4:5], v[56:57]
	v_pk_fma_f32 v[58:59], v[46:47], v[6:7], v[58:59]
	buffer_load_dwordx4 v[44:47], v64, s[0:3], s22 offen offset:3072 nt
	s_waitcnt vmcnt(9)
	v_pk_fma_f32 v[56:57], v[48:49], v[8:9], v[56:57]
	v_pk_fma_f32 v[58:59], v[50:51], v[10:11], v[58:59]
	buffer_load_dwordx4 v[48:51], v64, s[0:3], s23 offen nt
	s_waitcnt vmcnt(9)
	v_pk_fma_f32 v[56:57], v[52:53], v[12:13], v[56:57]
	v_pk_fma_f32 v[58:59], v[54:55], v[14:15], v[58:59]
	buffer_load_dwordx4 v[52:55], v64, s[0:3], s23 offen offset:1024 nt
	v_pk_add_f32 v[56:57], v[56:57], v[58:59]
	v_cmp_eq_u32_e32 vcc, 4, v63
	v_add_f32_e32 v60, v56, v57
	s_nop 1
	v_add_f32_dpp v60, v60, v60 quad_perm:[1,0,3,2] row_mask:0xf bank_mask:0xf bound_ctrl:1
	s_nop 1
	v_add_f32_dpp v60, v60, v60 quad_perm:[2,3,0,1] row_mask:0xf bank_mask:0xf bound_ctrl:1
	s_nop 1
	v_add_f32_dpp v60, v60, v60 row_ror:4 row_mask:0xf bank_mask:0xf bound_ctrl:1
	s_nop 1
	v_add_f32_dpp v60, v60, v60 row_ror:8 row_mask:0xf bank_mask:0xf bound_ctrl:1
	v_mov_b32_e32 v61, v60
	s_nop 1
	v_permlane16_swap_b32_e32 v60, v61
	v_add_f32_e32 v60, v60, v61
	v_mov_b32_e32 v61, v60
	s_nop 1
	v_permlane32_swap_b32_e32 v60, v61
	v_add_f32_e32 v60, v60, v61
	v_cndmask_b32_e32 v62, v62, v60, vcc
	s_waitcnt vmcnt(9)
	v_pk_mul_f32 v[56:57], v[16:17], v[0:1]
	v_pk_mul_f32 v[58:59], v[18:19], v[2:3]
	buffer_load_dwordx4 v[16:19], v64, s[0:3], s23 offen offset:2048 nt
	s_waitcnt vmcnt(9)
	v_pk_fma_f32 v[56:57], v[20:21], v[4:5], v[56:57]
	v_pk_fma_f32 v[58:59], v[22:23], v[6:7], v[58:59]
	buffer_load_dwordx4 v[20:23], v64, s[0:3], s23 offen offset:3072 nt
	s_waitcnt vmcnt(9)
	v_pk_fma_f32 v[56:57], v[24:25], v[8:9], v[56:57]
	v_pk_fma_f32 v[58:59], v[26:27], v[10:11], v[58:59]
	s_waitcnt vmcnt(8)
	v_pk_fma_f32 v[56:57], v[28:29], v[12:13], v[56:57]
	v_pk_fma_f32 v[58:59], v[30:31], v[14:15], v[58:59]
	s_nop 0
	v_pk_add_f32 v[56:57], v[56:57], v[58:59]
	v_cmp_eq_u32_e32 vcc, 5, v63
	v_add_f32_e32 v60, v56, v57
	s_nop 1
	v_add_f32_dpp v60, v60, v60 quad_perm:[1,0,3,2] row_mask:0xf bank_mask:0xf bound_ctrl:1
	s_nop 1
	v_add_f32_dpp v60, v60, v60 quad_perm:[2,3,0,1] row_mask:0xf bank_mask:0xf bound_ctrl:1
	s_nop 1
	v_add_f32_dpp v60, v60, v60 row_ror:4 row_mask:0xf bank_mask:0xf bound_ctrl:1
	s_nop 1
	v_add_f32_dpp v60, v60, v60 row_ror:8 row_mask:0xf bank_mask:0xf bound_ctrl:1
	v_mov_b32_e32 v61, v60
	s_nop 1
	v_permlane16_swap_b32_e32 v60, v61
	v_add_f32_e32 v60, v60, v61
	v_mov_b32_e32 v61, v60
	s_nop 1
	v_permlane32_swap_b32_e32 v60, v61
	v_add_f32_e32 v60, v60, v61
	v_cndmask_b32_e32 v62, v62, v60, vcc
	s_waitcnt vmcnt(7)
	v_pk_mul_f32 v[56:57], v[32:33], v[0:1]
	v_pk_mul_f32 v[58:59], v[34:35], v[2:3]
	s_waitcnt vmcnt(6)
	v_pk_fma_f32 v[56:57], v[36:37], v[4:5], v[56:57]
	v_pk_fma_f32 v[58:59], v[38:39], v[6:7], v[58:59]
	s_waitcnt vmcnt(5)
	v_pk_fma_f32 v[56:57], v[40:41], v[8:9], v[56:57]
	v_pk_fma_f32 v[58:59], v[42:43], v[10:11], v[58:59]
	s_waitcnt vmcnt(4)
	v_pk_fma_f32 v[56:57], v[44:45], v[12:13], v[56:57]
	v_pk_fma_f32 v[58:59], v[46:47], v[14:15], v[58:59]
	s_nop 0
	v_pk_add_f32 v[56:57], v[56:57], v[58:59]
	v_cmp_eq_u32_e32 vcc, 6, v63
	v_add_f32_e32 v60, v56, v57
	s_nop 1
	v_add_f32_dpp v60, v60, v60 quad_perm:[1,0,3,2] row_mask:0xf bank_mask:0xf bound_ctrl:1
	s_nop 1
	v_add_f32_dpp v60, v60, v60 quad_perm:[2,3,0,1] row_mask:0xf bank_mask:0xf bound_ctrl:1
	s_nop 1
	v_add_f32_dpp v60, v60, v60 row_ror:4 row_mask:0xf bank_mask:0xf bound_ctrl:1
	s_nop 1
	v_add_f32_dpp v60, v60, v60 row_ror:8 row_mask:0xf bank_mask:0xf bound_ctrl:1
	v_mov_b32_e32 v61, v60
	s_nop 1
	v_permlane16_swap_b32_e32 v60, v61
	v_add_f32_e32 v60, v60, v61
	v_mov_b32_e32 v61, v60
	s_nop 1
	v_permlane32_swap_b32_e32 v60, v61
	v_add_f32_e32 v60, v60, v61
	v_cndmask_b32_e32 v62, v62, v60, vcc
	s_waitcnt vmcnt(3)
	v_pk_mul_f32 v[56:57], v[48:49], v[0:1]
	v_pk_mul_f32 v[58:59], v[50:51], v[2:3]
	s_waitcnt vmcnt(2)
	v_pk_fma_f32 v[56:57], v[52:53], v[4:5], v[56:57]
	v_pk_fma_f32 v[58:59], v[54:55], v[6:7], v[58:59]
	s_waitcnt vmcnt(1)
	v_pk_fma_f32 v[56:57], v[16:17], v[8:9], v[56:57]
	v_pk_fma_f32 v[58:59], v[18:19], v[10:11], v[58:59]
	s_waitcnt vmcnt(0)
	v_pk_fma_f32 v[56:57], v[20:21], v[12:13], v[56:57]
	v_pk_fma_f32 v[58:59], v[22:23], v[14:15], v[58:59]
	s_nop 0
	v_pk_add_f32 v[56:57], v[56:57], v[58:59]
	v_cmp_eq_u32_e32 vcc, 7, v63
	v_add_f32_e32 v60, v56, v57
	s_nop 1
	v_add_f32_dpp v60, v60, v60 quad_perm:[1,0,3,2] row_mask:0xf bank_mask:0xf bound_ctrl:1
	s_nop 1
	v_add_f32_dpp v60, v60, v60 quad_perm:[2,3,0,1] row_mask:0xf bank_mask:0xf bound_ctrl:1
	s_nop 1
	v_add_f32_dpp v60, v60, v60 row_ror:4 row_mask:0xf bank_mask:0xf bound_ctrl:1
	s_nop 1
	v_add_f32_dpp v60, v60, v60 row_ror:8 row_mask:0xf bank_mask:0xf bound_ctrl:1
	v_mov_b32_e32 v61, v60
	s_nop 1
	v_permlane16_swap_b32_e32 v60, v61
	v_add_f32_e32 v60, v60, v61
	v_mov_b32_e32 v61, v60
	s_nop 1
	v_permlane32_swap_b32_e32 v60, v61
	v_add_f32_e32 v60, v60, v61
	v_cndmask_b32_e32 v62, v62, v60, vcc
	v_cmp_gt_u32_e32 vcc, 8, v63
	s_and_saveexec_b64 s[0:1], vcc
	v_lshlrev_b32_e32 v61, 2, v63
	s_lshl_b32 s9, s8, 13
	s_add_i32 s9, s9, s24
	s_addk_i32 s9, 0x6040
	v_add_u32_e32 v61, s9, v61
	global_store_dword v61, v62, s[6:7]
	s_endpgm

	.amdhsa_kernel _Z13stream_kernelPKfPf
		.amdhsa_group_segment_fixed_size 4096
		.amdhsa_private_segment_fixed_size 0
		.amdhsa_kernarg_size 16
		.amdhsa_user_sgpr_count 2
		.amdhsa_user_sgpr_dispatch_ptr 0
		.amdhsa_user_sgpr_queue_ptr 0
		.amdhsa_user_sgpr_kernarg_segment_ptr 1
		.amdhsa_user_sgpr_dispatch_id 0
		.amdhsa_user_sgpr_kernarg_preload_length 0
		.amdhsa_user_sgpr_kernarg_preload_offset 0
		.amdhsa_user_sgpr_private_segment_size 0
		.amdhsa_uses_dynamic_stack 0
		.amdhsa_enable_private_segment 0
		.amdhsa_system_sgpr_workgroup_id_x 1
		.amdhsa_system_sgpr_workgroup_id_y 0
		.amdhsa_system_sgpr_workgroup_id_z 0
		.amdhsa_system_sgpr_workgroup_info 0
		.amdhsa_system_vgpr_workitem_id 0
		.amdhsa_next_free_vgpr 65
		.amdhsa_next_free_sgpr 25
		.amdhsa_accum_offset 68
		.amdhsa_reserve_vcc 1
		.amdhsa_float_round_mode_32 0
		.amdhsa_float_round_mode_16_64 0
		.amdhsa_float_denorm_mode_32 3
		.amdhsa_float_denorm_mode_16_64 3
		.amdhsa_dx10_clamp 1
		.amdhsa_ieee_mode 1
		.amdhsa_fp16_overflow 0
		.amdhsa_tg_split 0
		.amdhsa_exception_fp_ieee_invalid_op 0
		.amdhsa_exception_fp_denorm_src 0
		.amdhsa_exception_fp_ieee_div_zero 0
		.amdhsa_exception_fp_ieee_overflow 0
		.amdhsa_exception_fp_ieee_underflow 0
		.amdhsa_exception_fp_ieee_inexact 0
		.amdhsa_exception_int_div_zero 0
	.end_amdhsa_kernel

.Lfunc_end1:
	.size	_Z13stream_kernelPKfPf, .Lfunc_end1-_Z13stream_kernelPKfPf
	.set _Z13stream_kernelPKfPf.num_vgpr, 65
	.set _Z13stream_kernelPKfPf.num_agpr, 0
	.set _Z13stream_kernelPKfPf.numbered_sgpr, 25
	.set _Z13stream_kernelPKfPf.num_named_barrier, 0
	.set _Z13stream_kernelPKfPf.private_seg_size, 0
	.set _Z13stream_kernelPKfPf.uses_vcc, 1
	.set _Z13stream_kernelPKfPf.uses_flat_scratch, 0
	.set _Z13stream_kernelPKfPf.has_dyn_sized_stack, 0
	.set _Z13stream_kernelPKfPf.has_recursion, 0
	.set _Z13stream_kernelPKfPf.has_indirect_call, 0

amdhsa.kernels:
  - .agpr_count:     0
    .args:
      - .actual_access:  read_only
        .address_space:  global
        .offset:         0
        .size:           8
        .value_kind:     global_buffer
      - .actual_access:  read_only
        .address_space:  global
        .offset:         8
        .size:           8
        .value_kind:     global_buffer
      - .actual_access:  read_only
        .address_space:  global
        .offset:         16
        .size:           8
        .value_kind:     global_buffer
      - .actual_access:  read_only
        .address_space:  global
        .offset:         24
        .size:           8
        .value_kind:     global_buffer
      - .actual_access:  write_only
        .address_space:  global
        .offset:         32
        .size:           8
        .value_kind:     global_buffer
    .group_segment_fixed_size: 2112
    .kernarg_segment_align: 8
    .kernarg_segment_size: 40
    .language:       OpenCL C
    .language_version:
      - 2
      - 0
    .max_flat_workgroup_size: 1024
    .name:           _Z11prep_kernelPKfS0_S0_S0_Pf
    .private_segment_fixed_size: 0
    .sgpr_count:     32
    .sgpr_spill_count: 0
    .symbol:         _Z11prep_kernelPKfS0_S0_S0_Pf.kd
    .uniform_work_group_size: 1
    .uses_dynamic_stack: false
    .vgpr_count:     40
    .vgpr_spill_count: 0
    .wavefront_size: 64
  - .agpr_count:     0
    .args:
      - .actual_access:  read_only
        .address_space:  global
        .offset:         0
        .size:           8
        .value_kind:     global_buffer
      - .address_space:  global
        .offset:         8
        .size:           8
        .value_kind:     global_buffer
    .group_segment_fixed_size: 4096
    .kernarg_segment_align: 8
    .kernarg_segment_size: 16
    .language:       OpenCL C
    .language_version:
      - 2
      - 0
    .max_flat_workgroup_size: 1024
    .name:           _Z13stream_kernelPKfPf
    .private_segment_fixed_size: 0
    .sgpr_count:     31
    .sgpr_spill_count: 0
    .symbol:         _Z13stream_kernelPKfPf.kd
    .uniform_work_group_size: 1
    .uses_dynamic_stack: false
    .vgpr_count:     65
    .vgpr_spill_count: 0
    .wavefront_size: 64
  - .agpr_count:     0
    .args:
      - .actual_access:  read_only
        .address_space:  global
        .offset:         0
        .size:           8
        .value_kind:     global_buffer
      - .actual_access:  write_only
        .address_space:  global
        .offset:         8
        .size:           8
        .value_kind:     global_buffer
    .group_segment_fixed_size: 32
    .kernarg_segment_align: 8
    .kernarg_segment_size: 16
    .language:       OpenCL C
    .language_version:
      - 2
      - 0
    .max_flat_workgroup_size: 256
    .name:           _Z14softmax_kernelPKfPf
    .private_segment_fixed_size: 0
    .sgpr_count:     16
    .sgpr_spill_count: 0
    .symbol:         _Z14softmax_kernelPKfPf.kd
    .uniform_work_group_size: 1
    .uses_dynamic_stack: false
    .vgpr_count:     17
    .vgpr_spill_count: 0
    .wavefront_size: 64
